# baseline (speedup 1.0000x reference)
.LBB0_86:
	s_or_b64 exec, exec, s[0:1]
	v_cmp_ne_u32_e32 vcc, 0, v14
	s_waitcnt lgkmcnt(0)
	s_barrier
	s_setprio 3
	v_and_b32_e32 v40, 15, v1
	v_lshrrev_b32_e32 v41, 4, v1
	s_and_b32 s44, s36, 1
	s_lshr_b32 s45, s36, 1
	s_mov_b32 s60, 0xffff
	s_mov_b32 s61, 0
	s_mov_b32 s62, 0xffff0000
	s_mov_b32 s63, 0
	s_mov_b32 s64, 0
	s_mov_b32 s65, 0xffff
	s_mov_b32 s66, 0
	s_mov_b32 s67, 0xffff0000
	v_cvt_pk_f16_f32 v2, v152, v153
	v_cvt_pk_f16_f32 v3, v154, v155
	v_cvt_pk_f16_f32 v4, v156, v157
	v_cvt_pk_f16_f32 v5, v158, v159
	s_lshl_b32 s46, s44, 3
	v_lshl_add_u32 v42, v41, 1, s46
	v_mul_u32_u24_e32 v32, 0x650, v42
	v_lshl_add_u32 v34, v40, 3, v32
	v_mul_u32_u24_e32 v33, 0x650, v40
	v_add_u32_e32 v33, 0x6500, v33
	s_lshl_b32 s47, s45, 1
	s_lshl_b32 s46, s44, 10
	s_add_i32 s47, s47, s46
	s_add_i32 s47, s47, 0x14b00
	v_lshl_add_u32 v39, v40, 2, s47
	v_lshl_add_u32 v39, v41, 8, v39
	v_lshlrev_b32_e32 v43, 4, v1
	v_add_u32_e32 v43, 0x14b00, v43
	v_lshlrev_b32_e32 v35, 4, v1
	v_mov_b32_e32 v44, 1
	s_lshl_b32 s46, s3, 2
	s_add_i32 s46, s46, s33
	s_mul_i32 s46, s46, 0x3200
	s_add_u32 s68, s26, s46
	s_addc_u32 s69, s27, 0
	s_mov_b32 s73, 0
	v_mov_b32_e32 v36, 0x14a00
